# P13 gather loop: at most 8 table gathers in flight per wave
# speedup vs baseline: 1.0250x; 1.0250x over previous
.LBB0_1456:
	v_lshl_add_u32 v3, s0, 9, v162
	ds_read2_b32 v[4:5], v3 offset0:64 offset1:68
	ds_read2_b32 v[78:79], v3 offset0:72 offset1:76
	v_mov_b32_e32 v177, 0
	s_waitcnt vmcnt(2)
	v_dot4c_i32_i8_e32 v177, v6, v10
	v_dot4c_i32_i8_e32 v177, v7, v11
	s_waitcnt lgkmcnt(1)
	v_lshl_or_b32 v4, v4, 8, v144
	v_lshl_or_b32 v5, v5, 8, v144
	s_waitcnt vmcnt(0)
	global_load_dwordx4 v[138:141], v4, s[26:27]
	global_load_dwordx4 v[134:137], v5, s[26:27]
	ds_read2_b32 v[4:5], v3 offset0:80 offset1:84
	s_waitcnt lgkmcnt(1)
	v_lshl_or_b32 v78, v78, 8, v144
	v_lshl_or_b32 v79, v79, 8, v144
	global_load_dwordx4 v[130:133], v78, s[26:27]
	global_load_dwordx4 v[122:125], v79, s[26:27]
	ds_read2_b32 v[78:79], v3 offset0:88 offset1:92
	s_waitcnt lgkmcnt(1)
	v_lshl_or_b32 v4, v4, 8, v144
	v_lshl_or_b32 v5, v5, 8, v144
	global_load_dwordx4 v[126:129], v4, s[26:27]
	global_load_dwordx4 v[118:121], v5, s[26:27]
	ds_read2_b32 v[4:5], v3 offset0:96 offset1:100
	s_waitcnt lgkmcnt(1)
	v_lshl_or_b32 v78, v78, 8, v144
	v_lshl_or_b32 v79, v79, 8, v144
	global_load_dwordx4 v[114:117], v78, s[26:27]
	global_load_dwordx4 v[106:109], v79, s[26:27]
	s_waitcnt vmcnt(0)
	ds_read2_b32 v[78:79], v3 offset0:104 offset1:108
	s_waitcnt lgkmcnt(1)
	v_lshl_or_b32 v4, v4, 8, v144
	v_lshl_or_b32 v5, v5, 8, v144
	global_load_dwordx4 v[110:113], v4, s[26:27]
	global_load_dwordx4 v[102:105], v5, s[26:27]
	ds_read2_b32 v[4:5], v3 offset0:112 offset1:116
	s_waitcnt lgkmcnt(1)
	v_lshl_or_b32 v78, v78, 8, v144
	v_lshl_or_b32 v79, v79, 8, v144
	global_load_dwordx4 v[98:101], v78, s[26:27]
	global_load_dwordx4 v[90:93], v79, s[26:27]
	ds_read2_b32 v[78:79], v3 offset0:120 offset1:124
	s_waitcnt lgkmcnt(1)
	v_lshl_or_b32 v3, v4, 8, v144
	v_lshl_or_b32 v4, v5, 8, v144
	global_load_dwordx4 v[94:97], v3, s[26:27]
	global_load_dwordx4 v[86:89], v4, s[26:27]
	v_dot4c_i32_i8_e32 v177, v8, v12
	s_waitcnt lgkmcnt(0)
	v_lshl_or_b32 v3, v78, 8, v144
	v_lshl_or_b32 v4, v79, 8, v144
	global_load_dwordx4 v[82:85], v3, s[26:27]
	global_load_dwordx4 v[78:81], v4, s[26:27]
	s_waitcnt vmcnt(0)
	s_waitcnt lgkmcnt(0)
	v_lshl_add_u32 v4, s36, 2, v162
	v_lshl_add_u32 v8, s36, 2, v162
	ds_read_b32 v6, v4
	v_dot4c_i32_i8_e32 v177, v9, v13
	ds_read_b32 v9, v8 offset:240
	ds_read2_b32 v[4:5], v8 offset0:4 offset1:8
	v_mov_b32_e32 v3, 0
	v_mov_b32_e32 v163, 0
	s_waitcnt vmcnt(16)
	v_dot4c_i32_i8_e32 v3, v74, v10
	v_dot4c_i32_i8_e32 v163, v70, v10
	v_dot4c_i32_i8_e32 v3, v75, v11
	v_dot4c_i32_i8_e32 v163, v71, v11
	v_mov_b32_e32 v176, 0
	v_dot4c_i32_i8_e32 v3, v76, v12
	v_dot4c_i32_i8_e32 v163, v72, v12
	v_dot4c_i32_i8_e32 v176, v14, v10
	s_waitcnt lgkmcnt(2)
	v_lshl_or_b32 v14, v6, 8, v144
	ds_read2_b32 v[6:7], v8 offset0:12 offset1:16
	s_waitcnt lgkmcnt(1)
	v_lshl_or_b32 v4, v4, 8, v144
	v_dot4c_i32_i8_e32 v3, v77, v13
	v_dot4c_i32_i8_e32 v163, v73, v13
	s_waitcnt vmcnt(0)
	global_load_dwordx4 v[74:77], v14, s[26:27]
	global_load_dwordx4 v[70:73], v4, s[26:27]
	v_lshl_or_b32 v14, v5, 8, v144
	ds_read2_b32 v[4:5], v8 offset0:20 offset1:24
	v_mov_b32_e32 v164, 0
	v_mov_b32_e32 v165, 0
	v_dot4c_i32_i8_e32 v164, v66, v10
	v_dot4c_i32_i8_e32 v165, v62, v10
	v_mov_b32_e32 v166, 0
	v_mov_b32_e32 v167, 0
	v_dot4c_i32_i8_e32 v164, v67, v11
	v_dot4c_i32_i8_e32 v165, v63, v11
	v_dot4c_i32_i8_e32 v166, v58, v10
	v_dot4c_i32_i8_e32 v167, v54, v10
	v_dot4c_i32_i8_e32 v164, v68, v12
	v_dot4c_i32_i8_e32 v165, v64, v12
	v_dot4c_i32_i8_e32 v166, v59, v11
	v_dot4c_i32_i8_e32 v167, v55, v11
	s_waitcnt lgkmcnt(1)
	v_lshl_or_b32 v6, v6, 8, v144
	v_dot4c_i32_i8_e32 v164, v69, v13
	v_dot4c_i32_i8_e32 v165, v65, v13
	v_dot4c_i32_i8_e32 v166, v60, v12
	v_dot4c_i32_i8_e32 v167, v56, v12
	s_waitcnt vmcnt(0)
	global_load_dwordx4 v[66:69], v14, s[26:27]
	global_load_dwordx4 v[62:65], v6, s[26:27]
	v_lshl_or_b32 v14, v7, 8, v144
	s_waitcnt lgkmcnt(0)
	v_lshl_or_b32 v4, v4, 8, v144
	ds_read2_b32 v[6:7], v8 offset0:28 offset1:32
	v_dot4c_i32_i8_e32 v166, v61, v13
	v_dot4c_i32_i8_e32 v167, v57, v13
	global_load_dwordx4 v[58:61], v14, s[26:27]
	global_load_dwordx4 v[54:57], v4, s[26:27]
	v_lshl_or_b32 v14, v5, 8, v144
	ds_read2_b32 v[4:5], v8 offset0:36 offset1:40
	v_mov_b32_e32 v168, 0
	v_mov_b32_e32 v169, 0
	v_dot4c_i32_i8_e32 v168, v50, v10
	v_dot4c_i32_i8_e32 v169, v46, v10
	v_mov_b32_e32 v170, 0
	v_mov_b32_e32 v171, 0
	v_dot4c_i32_i8_e32 v168, v51, v11
	v_dot4c_i32_i8_e32 v169, v47, v11
	v_dot4c_i32_i8_e32 v170, v42, v10
	v_dot4c_i32_i8_e32 v171, v38, v10
	v_dot4c_i32_i8_e32 v168, v52, v12
	v_dot4c_i32_i8_e32 v169, v48, v12
	v_dot4c_i32_i8_e32 v170, v43, v11
	v_dot4c_i32_i8_e32 v171, v39, v11
	s_waitcnt lgkmcnt(1)
	v_lshl_or_b32 v6, v6, 8, v144
	v_dot4c_i32_i8_e32 v168, v53, v13
	v_dot4c_i32_i8_e32 v169, v49, v13
	v_dot4c_i32_i8_e32 v170, v44, v12
	v_dot4c_i32_i8_e32 v171, v40, v12
	s_waitcnt vmcnt(0)
	global_load_dwordx4 v[50:53], v14, s[26:27]
	global_load_dwordx4 v[46:49], v6, s[26:27]
	v_lshl_or_b32 v14, v7, 8, v144
	s_waitcnt lgkmcnt(0)
	v_lshl_or_b32 v4, v4, 8, v144
	ds_read2_b32 v[6:7], v8 offset0:44 offset1:48
	v_dot4c_i32_i8_e32 v170, v45, v13
	v_dot4c_i32_i8_e32 v171, v41, v13
	global_load_dwordx4 v[42:45], v14, s[26:27]
	global_load_dwordx4 v[38:41], v4, s[26:27]
	v_lshl_or_b32 v14, v5, 8, v144
	ds_read2_b32 v[4:5], v8 offset0:52 offset1:56
	v_mov_b32_e32 v172, 0
	v_mov_b32_e32 v173, 0
	v_dot4c_i32_i8_e32 v172, v34, v10
	v_dot4c_i32_i8_e32 v173, v30, v10
	v_mov_b32_e32 v174, 0
	v_mov_b32_e32 v175, 0
	v_dot4c_i32_i8_e32 v172, v35, v11
	v_dot4c_i32_i8_e32 v173, v31, v11
	v_dot4c_i32_i8_e32 v174, v26, v10
	v_dot4c_i32_i8_e32 v175, v22, v10
	v_dot4c_i32_i8_e32 v172, v36, v12
	v_dot4c_i32_i8_e32 v173, v32, v12
	v_dot4c_i32_i8_e32 v174, v27, v11
	v_dot4c_i32_i8_e32 v175, v23, v11
	s_waitcnt lgkmcnt(1)
	v_lshl_or_b32 v6, v6, 8, v144
	v_dot4c_i32_i8_e32 v172, v37, v13
	v_dot4c_i32_i8_e32 v173, v33, v13
	v_dot4c_i32_i8_e32 v174, v28, v12
	v_dot4c_i32_i8_e32 v175, v24, v12
	v_dot4c_i32_i8_e32 v176, v15, v11
	s_waitcnt vmcnt(0)
	global_load_dwordx4 v[34:37], v14, s[26:27]
	global_load_dwordx4 v[30:33], v6, s[26:27]
	v_lshl_or_b32 v6, v7, 8, v144
	s_waitcnt lgkmcnt(0)
	v_lshl_or_b32 v4, v4, 8, v144
	v_dot4c_i32_i8_e32 v174, v29, v13
	v_dot4c_i32_i8_e32 v175, v25, v13
	v_dot4c_i32_i8_e32 v176, v16, v12
	global_load_dwordx4 v[26:29], v6, s[26:27]
	global_load_dwordx4 v[22:25], v4, s[26:27]
	v_lshl_or_b32 v4, v5, 8, v144
	v_dot4c_i32_i8_e32 v176, v17, v13
	v_lshl_or_b32 v5, v9, 8, v144
	global_load_dwordx4 v[14:17], v4, s[26:27]
	global_load_dwordx4 v[6:9], v5, s[26:27]
	v_mov_b32_e32 v5, 0
	s_waitcnt vmcnt(30)
	v_dot4c_i32_i8_e32 v5, v134, v10
	v_mov_b32_e32 v134, 0
	s_waitcnt vmcnt(29)
	v_dot4c_i32_i8_e32 v134, v130, v10
	v_mov_b32_e32 v130, 0
	s_waitcnt vmcnt(28)
	v_dot4c_i32_i8_e32 v130, v122, v10
	v_dot4c_i32_i8_e32 v130, v123, v11
	v_mov_b32_e32 v123, 0
	s_waitcnt vmcnt(26)
	v_dot4c_i32_i8_e32 v123, v118, v10
	v_mov_b32_e32 v118, 0
	s_waitcnt vmcnt(25)
	v_dot4c_i32_i8_e32 v118, v114, v10
	v_mov_b32_e32 v114, 0
	s_waitcnt vmcnt(24)
	v_dot4c_i32_i8_e32 v114, v106, v10
	v_dot4c_i32_i8_e32 v114, v107, v11
	v_mov_b32_e32 v107, 0
	s_waitcnt vmcnt(22)
	v_dot4c_i32_i8_e32 v107, v102, v10
	v_mov_b32_e32 v102, 0
	v_mov_b32_e32 v4, 0
	s_waitcnt vmcnt(21)
	v_dot4c_i32_i8_e32 v102, v98, v10
	v_mov_b32_e32 v98, 0
	v_dot4c_i32_i8_e32 v4, v138, v10
	s_waitcnt vmcnt(20)
	v_dot4c_i32_i8_e32 v98, v90, v10
	v_dot4c_i32_i8_e32 v4, v139, v11
	v_dot4c_i32_i8_e32 v5, v135, v11
	v_dot4c_i32_i8_e32 v98, v91, v11
	v_mov_b32_e32 v91, 0
	v_dot4c_i32_i8_e32 v4, v140, v12
	v_dot4c_i32_i8_e32 v5, v136, v12
	v_dot4c_i32_i8_e32 v134, v131, v11
	v_mov_b32_e32 v122, 0
	s_waitcnt vmcnt(18)
	v_dot4c_i32_i8_e32 v91, v86, v10
	v_mov_b32_e32 v86, 0
	v_dot4c_i32_i8_e32 v4, v141, v13
	v_dot4c_i32_i8_e32 v5, v137, v13
	v_dot4c_i32_i8_e32 v134, v132, v12
	v_dot4c_i32_i8_e32 v122, v126, v10
	v_mov_b32_e32 v106, 0
	v_mov_b32_e32 v90, 0
	s_waitcnt vmcnt(17)
	v_dot4c_i32_i8_e32 v86, v82, v10
	v_mov_b32_e32 v82, 0
	v_dot4c_i32_i8_e32 v134, v133, v13
	v_dot4c_i32_i8_e32 v130, v124, v12
	v_dot4c_i32_i8_e32 v122, v127, v11
	v_dot4c_i32_i8_e32 v106, v110, v10
	v_dot4c_i32_i8_e32 v90, v94, v10
	s_waitcnt vmcnt(16)
	v_dot4c_i32_i8_e32 v82, v78, v10
	v_cndmask_b32_e64 v10, v3, v4, s[6:7]
	v_cndmask_b32_e64 v3, v4, v3, s[6:7]
	v_cndmask_b32_e64 v4, v163, v5, s[6:7]
	v_cndmask_b32_e64 v5, v5, v163, s[6:7]
	v_dot4c_i32_i8_e32 v130, v125, v13
	v_dot4c_i32_i8_e32 v122, v128, v12
	v_dot4c_i32_i8_e32 v123, v119, v11
	v_add_u32_dpp v3, v10, v3 row_ror:8 row_mask:0xf bank_mask:0xf bound_ctrl:1
	v_add_u32_dpp v4, v4, v5 row_ror:8 row_mask:0xf bank_mask:0xf bound_ctrl:1
	v_cndmask_b32_e64 v5, v164, v134, s[6:7]
	v_cndmask_b32_e64 v10, v134, v164, s[6:7]
	v_dot4c_i32_i8_e32 v122, v129, v13
	v_dot4c_i32_i8_e32 v123, v120, v12
	v_dot4c_i32_i8_e32 v118, v115, v11
	v_dot4c_i32_i8_e32 v106, v111, v11
	v_dot4c_i32_i8_e32 v107, v103, v11
	v_dot4c_i32_i8_e32 v102, v99, v11
	v_dot4c_i32_i8_e32 v90, v95, v11
	v_dot4c_i32_i8_e32 v91, v87, v11
	v_dot4c_i32_i8_e32 v86, v83, v11
	v_dot4c_i32_i8_e32 v82, v79, v11
	v_add_u32_dpp v5, v5, v10 row_ror:8 row_mask:0xf bank_mask:0xf bound_ctrl:1
	v_cndmask_b32_e64 v10, v165, v130, s[6:7]
	v_cndmask_b32_e64 v11, v130, v165, s[6:7]
	v_dot4c_i32_i8_e32 v123, v121, v13
	v_dot4c_i32_i8_e32 v118, v116, v12
	v_dot4c_i32_i8_e32 v114, v108, v12
	v_dot4c_i32_i8_e32 v106, v112, v12
	v_dot4c_i32_i8_e32 v107, v104, v12
	v_dot4c_i32_i8_e32 v102, v100, v12
	v_dot4c_i32_i8_e32 v98, v92, v12
	v_dot4c_i32_i8_e32 v90, v96, v12
	v_dot4c_i32_i8_e32 v91, v88, v12
	v_dot4c_i32_i8_e32 v86, v84, v12
	v_dot4c_i32_i8_e32 v82, v80, v12
	v_add_u32_dpp v10, v10, v11 row_ror:8 row_mask:0xf bank_mask:0xf bound_ctrl:1
	v_cndmask_b32_e64 v11, v166, v122, s[6:7]
	v_cndmask_b32_e64 v12, v122, v166, s[6:7]
	v_dot4c_i32_i8_e32 v118, v117, v13
	v_dot4c_i32_i8_e32 v114, v109, v13
	v_dot4c_i32_i8_e32 v106, v113, v13
	v_dot4c_i32_i8_e32 v107, v105, v13
	v_dot4c_i32_i8_e32 v102, v101, v13
	v_dot4c_i32_i8_e32 v98, v93, v13
	v_dot4c_i32_i8_e32 v90, v97, v13
	v_dot4c_i32_i8_e32 v91, v89, v13
	v_dot4c_i32_i8_e32 v86, v85, v13
	v_dot4c_i32_i8_e32 v82, v81, v13
	v_add_u32_dpp v11, v11, v12 row_ror:8 row_mask:0xf bank_mask:0xf bound_ctrl:1
	v_cndmask_b32_e64 v12, v167, v123, s[6:7]
	v_cndmask_b32_e64 v13, v123, v167, s[6:7]
	v_cndmask_b32_e64 v78, v118, v168, s[6:7]
	v_cndmask_b32_e64 v79, v114, v169, s[6:7]
	v_add_u32_dpp v12, v12, v13 row_ror:8 row_mask:0xf bank_mask:0xf bound_ctrl:1
	v_cndmask_b32_e64 v13, v168, v118, s[6:7]
	v_cndmask_b32_e64 v80, v106, v170, s[6:7]
	v_cndmask_b32_e64 v81, v107, v171, s[6:7]
	v_add_u32_dpp v13, v13, v78 row_ror:8 row_mask:0xf bank_mask:0xf bound_ctrl:1
	v_cndmask_b32_e64 v78, v169, v114, s[6:7]
	v_cndmask_b32_e64 v83, v102, v172, s[6:7]
	v_cndmask_b32_e64 v84, v98, v173, s[6:7]
	v_add_u32_dpp v78, v78, v79 row_ror:8 row_mask:0xf bank_mask:0xf bound_ctrl:1
	v_cndmask_b32_e64 v79, v170, v106, s[6:7]
	v_cndmask_b32_e64 v85, v90, v174, s[6:7]
	v_cndmask_b32_e64 v87, v91, v175, s[6:7]
	v_add_u32_dpp v79, v79, v80 row_ror:8 row_mask:0xf bank_mask:0xf bound_ctrl:1
	v_cndmask_b32_e64 v80, v171, v107, s[6:7]
	s_xor_b32 s0, s0, 1
	v_lshl_add_u64 v[160:161], v[160:161], 0, s[22:23]
	v_add_u32_dpp v80, v80, v81 row_ror:8 row_mask:0xf bank_mask:0xf bound_ctrl:1
	v_cndmask_b32_e64 v81, v172, v102, s[6:7]
	s_andn2_b64 vcc, exec, s[28:29]
	s_mov_b32 s37, s5
	v_add_u32_dpp v81, v81, v83 row_ror:8 row_mask:0xf bank_mask:0xf bound_ctrl:1
	v_cndmask_b32_e64 v83, v173, v98, s[6:7]
	s_nop 1
	v_add_u32_dpp v83, v83, v84 row_ror:8 row_mask:0xf bank_mask:0xf bound_ctrl:1
	v_cndmask_b32_e64 v84, v174, v90, s[6:7]
	s_nop 1
	v_add_u32_dpp v84, v84, v85 row_ror:8 row_mask:0xf bank_mask:0xf bound_ctrl:1
	v_cndmask_b32_e64 v85, v175, v91, s[6:7]
	s_nop 1
	v_add_u32_dpp v85, v85, v87 row_ror:8 row_mask:0xf bank_mask:0xf bound_ctrl:1
	v_cndmask_b32_e64 v87, v176, v86, s[6:7]
	v_cndmask_b32_e64 v86, v86, v176, s[6:7]
	s_nop 1
	v_add_u32_dpp v86, v87, v86 row_ror:8 row_mask:0xf bank_mask:0xf bound_ctrl:1
	v_cndmask_b32_e64 v87, v177, v82, s[6:7]
	v_cndmask_b32_e64 v82, v82, v177, s[6:7]
	s_nop 1
	v_add_u32_dpp v82, v87, v82 row_ror:8 row_mask:0xf bank_mask:0xf bound_ctrl:1
	v_cndmask_b32_e64 v87, v3, v79, s[8:9]
	v_cndmask_b32_e64 v3, v79, v3, s[8:9]
	v_cndmask_b32_e64 v79, v4, v80, s[8:9]
	v_cndmask_b32_e64 v4, v80, v4, s[8:9]
	v_add_u32_dpp v3, v87, v3 row_half_mirror row_mask:0xf bank_mask:0xf bound_ctrl:1
	s_nop 0
	v_add_u32_dpp v4, v79, v4 row_half_mirror row_mask:0xf bank_mask:0xf bound_ctrl:1
	v_cndmask_b32_e64 v79, v5, v81, s[8:9]
	v_cndmask_b32_e64 v5, v81, v5, s[8:9]
	s_nop 1
	v_add_u32_dpp v5, v79, v5 row_half_mirror row_mask:0xf bank_mask:0xf bound_ctrl:1
	v_cndmask_b32_e64 v79, v10, v83, s[8:9]
	v_cndmask_b32_e64 v10, v83, v10, s[8:9]
	s_nop 1
	v_add_u32_dpp v10, v79, v10 row_half_mirror row_mask:0xf bank_mask:0xf bound_ctrl:1
	v_cndmask_b32_e64 v79, v11, v84, s[8:9]
	v_cndmask_b32_e64 v11, v84, v11, s[8:9]
	s_nop 1
	v_add_u32_dpp v11, v79, v11 row_half_mirror row_mask:0xf bank_mask:0xf bound_ctrl:1
	v_cndmask_b32_e64 v79, v12, v85, s[8:9]
	v_cndmask_b32_e64 v12, v85, v12, s[8:9]
	s_nop 1
	v_add_u32_dpp v12, v79, v12 row_half_mirror row_mask:0xf bank_mask:0xf bound_ctrl:1
	v_cndmask_b32_e64 v79, v13, v86, s[8:9]
	v_cndmask_b32_e64 v13, v86, v13, s[8:9]
	s_nop 1
	v_add_u32_dpp v13, v79, v13 row_half_mirror row_mask:0xf bank_mask:0xf bound_ctrl:1
	v_cndmask_b32_e64 v79, v78, v82, s[8:9]
	v_cndmask_b32_e64 v78, v82, v78, s[8:9]
	s_nop 1
	v_add_u32_dpp v78, v79, v78 row_half_mirror row_mask:0xf bank_mask:0xf bound_ctrl:1
	v_cndmask_b32_e64 v79, v3, v11, s[10:11]
	v_cndmask_b32_e64 v3, v11, v3, s[10:11]
	v_cndmask_b32_e64 v11, v4, v12, s[10:11]
	v_cndmask_b32_e64 v4, v12, v4, s[10:11]
	v_add_u32_dpp v3, v79, v3 quad_perm:[2,3,0,1] row_mask:0xf bank_mask:0xf bound_ctrl:1
	s_nop 0
	v_add_u32_dpp v4, v11, v4 quad_perm:[2,3,0,1] row_mask:0xf bank_mask:0xf bound_ctrl:1
	v_cndmask_b32_e64 v11, v5, v13, s[10:11]
	v_cndmask_b32_e64 v5, v13, v5, s[10:11]
	s_nop 1
	v_add_u32_dpp v5, v11, v5 quad_perm:[2,3,0,1] row_mask:0xf bank_mask:0xf bound_ctrl:1
	v_cndmask_b32_e64 v11, v10, v78, s[10:11]
	v_cndmask_b32_e64 v10, v78, v10, s[10:11]
	s_nop 1
	v_add_u32_dpp v10, v11, v10 quad_perm:[2,3,0,1] row_mask:0xf bank_mask:0xf bound_ctrl:1
	v_cndmask_b32_e64 v11, v3, v5, s[12:13]
	v_cndmask_b32_e64 v3, v5, v3, s[12:13]
	v_cndmask_b32_e64 v5, v4, v10, s[12:13]
	v_cndmask_b32_e64 v4, v10, v4, s[12:13]
	v_add_u32_dpp v3, v11, v3 quad_perm:[1,0,3,2] row_mask:0xf bank_mask:0xf bound_ctrl:1
	v_cvt_f32_i32_e32 v3, v3
	v_add_u32_dpp v4, v5, v4 quad_perm:[1,0,3,2] row_mask:0xf bank_mask:0xf bound_ctrl:1
	v_cvt_f32_i32_e32 v4, v4
	v_mov_b64_e32 v[10:11], v[18:19]
	global_store_dword v[158:159], v3, off
	global_store_dword v[158:159], v4, off offset:16
	v_lshl_add_u64 v[158:159], v[158:159], 0, s[20:21]
	v_mov_b64_e32 v[12:13], v[20:21]
	s_cbranch_vccz .LBB0_1450
